# P6 first key block: all 16 Q/K fragment loads issued together, and the five late V fragment loads moved ahead of the softplus block into spare registers
# speedup vs baseline: 1.0002x; 1.0002x over previous
.LBB0_1661:
	s_or_b64 exec, exec, s[42:43]
	v_readfirstlane_b32 s42, v2
	s_mul_i32 s62, s42, s48
	s_add_i32 s62, s62, s2
	s_cmpk_gt_i32 s62, 0x1fff
	s_mov_b64 s[42:43], -1
	s_cbranch_scc1 .LBB0_1656
	s_ashr_i32 s42, s62, 5
	s_sub_i32 s43, 0xff, s42
	s_lshl_b32 s63, s62, 10
	s_lshl_b32 s58, s43, 5
	s_and_b32 s63, s63, 0x6000
	s_add_i32 s58, s58, s63
	v_or_b32_e32 v148, s58, v1
	s_lshl_b32 s58, s62, 7
	s_lshl_b32 s62, s62, 8
	s_and_b32 s62, s62, 0x1f00
	s_add_i32 s64, s62, s43
	s_mov_b32 s65, s59
	s_lshl_b64 s[64:65], s[64:65], 13
	v_mov_b64_e32 v[6:7], s[44:45]
	s_and_b32 s58, s58, 0x380
	s_waitcnt vmcnt(1)
	v_lshl_add_u64 v[30:31], v[140:141], 0, s[64:65]
	v_mad_u64_u32 v[6:7], s[72:73], v148, s53, v[6:7]
	global_load_dwordx4 v[2:5], v[30:31], off
	s_lshl_b32 s72, s58, 1
	s_mov_b32 s73, s59
	v_lshl_add_u64 v[6:7], v[6:7], 0, s[72:73]
	v_mov_b32_e32 v147, v139
	v_lshl_add_u64 v[6:7], v[6:7], 0, v[146:147]
	v_add_co_u32_e32 v8, vcc, s67, v6
	v_lshl_add_u64 v[36:37], v[6:7], 0, s[60:61]
	s_nop 0
	v_addc_co_u32_e32 v9, vcc, 0, v7, vcc
	global_load_dwordx4 v[82:85], v[8:9], off offset:3072
	global_load_dwordx4 v[18:21], v[30:31], off offset:1024
	global_load_dwordx4 v[86:89], v[36:37], off offset:32
	global_load_dwordx4 v[22:25], v[30:31], off offset:2048
	global_load_dwordx4 v[90:93], v[36:37], off offset:64
	global_load_dwordx4 v[26:29], v[30:31], off offset:3072
	global_load_dwordx4 v[94:97], v[36:37], off offset:96
	v_add_co_u32_e32 v30, vcc, s49, v30
	s_nop 1
	v_addc_co_u32_e32 v31, vcc, 0, v31, vcc
	global_load_dwordx4 v[220:223], v[30:31], off
	global_load_dwordx4 v[98:101], v[36:37], off offset:128
	global_load_dwordx4 v[224:227], v[30:31], off offset:1024
	global_load_dwordx4 v[102:105], v[36:37], off offset:160
	global_load_dwordx4 v[228:231], v[30:31], off offset:2048
	global_load_dwordx4 v[106:109], v[36:37], off offset:192
	global_load_dwordx4 v[32:35], v[30:31], off offset:3072
	global_load_dwordx4 v[110:113], v[36:37], off offset:224
	s_waitcnt vmcnt(14)
	v_mfma_f32_32x32x16_bf16 v[2:17], v[2:5], v[82:85], 0
	s_waitcnt vmcnt(12)
	v_mfma_f32_32x32x16_bf16 v[2:17], v[18:21], v[86:89], v[2:17]
	s_waitcnt vmcnt(10)
	v_mfma_f32_32x32x16_bf16 v[2:17], v[22:25], v[90:93], v[2:17]
	s_waitcnt vmcnt(8)
	v_mfma_f32_32x32x16_bf16 v[2:17], v[26:29], v[94:97], v[2:17]
	s_waitcnt vmcnt(6)
	v_mfma_f32_32x32x16_bf16 v[2:17], v[220:223], v[98:101], v[2:17]
	v_lshl_add_u64 v[30:31], v[142:143], 0, s[64:65]
	s_waitcnt vmcnt(4)
	v_mfma_f32_32x32x16_bf16 v[2:17], v[224:227], v[102:105], v[2:17]
	s_waitcnt vmcnt(2)
	v_mfma_f32_32x32x16_bf16 v[2:17], v[228:231], v[106:109], v[2:17]
	global_load_dwordx4 v[26:29], v[30:31], off
	global_load_dwordx4 v[22:25], v[30:31], off offset:1024
	global_load_dwordx4 v[18:21], v[30:31], off offset:2048
	s_waitcnt vmcnt(3)
	v_mfma_f32_32x32x16_bf16 v[2:17], v[32:35], v[110:113], v[2:17]
	s_mov_b32 s92, s49
	s_mov_b32 s93, 0
	v_lshl_add_u64 v[252:253], v[30:31], 0, s[92:93]
	global_load_dwordx4 v[244:247], v[30:31], off offset:3072
	global_load_dwordx4 v[248:251], v[252:253], off
	global_load_dwordx4 v[232:235], v[252:253], off offset:3072
	global_load_dwordx4 v[236:239], v[252:253], off offset:1024
	global_load_dwordx4 v[240:243], v[252:253], off offset:2048
	s_nop 11
	v_mul_f32_e32 v32, 0x3e0293ee, v2
	v_exp_f32_e64 v46, -|v32|
	v_mul_f32_e32 v34, 0x3e0293ee, v4
	v_mul_f32_e32 v33, 0x3e0293ee, v3
	v_mul_f32_e32 v36, 0x3e0293ee, v6
	v_mul_f32_e32 v38, 0x3e0293ee, v8
	v_exp_f32_e64 v48, -|v34|
	v_mul_f32_e32 v37, 0x3e0293ee, v7
	v_exp_f32_e64 v47, -|v33|
	v_exp_f32_e64 v50, -|v36|
	v_exp_f32_e64 v52, -|v38|
	v_add_f32_e32 v46, 1.0, v46
	v_mul_f32_e32 v39, 0x3e0293ee, v9
	v_mul_f32_e32 v45, 0x3e0293ee, v15
	v_exp_f32_e64 v51, -|v37|
	v_log_f32_e32 v46, v46
	v_exp_f32_e64 v53, -|v39|
	v_exp_f32_e64 v59, -|v45|
	v_add_f32_e32 v48, 1.0, v48
	v_max_f32_e32 v32, 0, v32
	v_add_f32_e32 v47, 1.0, v47
	v_add_f32_e32 v50, 1.0, v50
	v_add_f32_e32 v52, 1.0, v52
	v_log_f32_e32 v48, v48
	v_mul_f32_e32 v44, 0x3e0293ee, v14
	v_add_f32_e32 v51, 1.0, v51
	v_log_f32_e32 v47, v47
	v_log_f32_e32 v50, v50
	v_log_f32_e32 v52, v52
	v_add_f32_e32 v32, v32, v46
	v_exp_f32_e64 v58, -|v44|
	v_add_f32_e32 v53, 1.0, v53
	v_log_f32_e32 v51, v51
	v_cndmask_b32_e64 v46, 0, -v32, s[8:9]
	v_fma_f32 v32, v2, s68, -v32
	v_add_f32_e32 v2, 1.0, v59
	v_max_f32_e32 v34, 0, v34
	v_log_f32_e32 v53, v53
	v_log_f32_e32 v2, v2
	v_max_f32_e32 v33, 0, v33
	v_max_f32_e32 v36, 0, v36
	v_max_f32_e32 v38, 0, v38
	v_add_f32_e32 v34, v34, v48
	v_max_f32_e32 v37, 0, v37
	v_add_f32_e32 v33, v33, v47
	v_add_f32_e32 v36, v36, v50
	v_add_f32_e32 v38, v38, v52
	v_cndmask_b32_e64 v48, 0, -v34, s[12:13]
	v_fma_f32 v34, v4, s68, -v34
	v_mul_f32_e32 v4, 0x3e0293ee, v16
	v_mul_f32_e32 v35, 0x3e0293ee, v5
	v_max_f32_e32 v39, 0, v39
	v_add_f32_e32 v58, 1.0, v58
	v_add_f32_e32 v37, v37, v51
	v_cndmask_b32_e64 v47, 0, -v33, s[10:11]
	v_fma_f32 v33, v3, s68, -v33
	v_cndmask_b32_e64 v3, 0, -v36, s[16:17]
	v_fma_f32 v36, v6, s68, -v36
	v_cndmask_b32_e64 v51, 0, -v38, s[20:21]
	v_fma_f32 v38, v8, s68, -v38
	v_exp_f32_e64 v6, -|v4|
	v_max_f32_e32 v8, 0, v45
	v_exp_f32_e64 v49, -|v35|
	v_log_f32_e32 v58, v58
	v_add_f32_e32 v39, v39, v53
	v_add_f32_e32 v2, v8, v2
	v_mul_f32_e32 v8, 0x3e0293ee, v17
	v_mul_f32_e32 v40, 0x3e0293ee, v10
	v_mul_f32_e32 v41, 0x3e0293ee, v11
	v_mul_f32_e32 v42, 0x3e0293ee, v12
	v_mul_f32_e32 v43, 0x3e0293ee, v13
	v_cndmask_b32_e64 v52, 0, -v39, s[22:23]
	v_fma_f32 v39, v9, s68, -v39
	v_exp_f32_e64 v9, -|v8|
	v_exp_f32_e64 v54, -|v40|
	v_exp_f32_e64 v55, -|v41|
	v_exp_f32_e64 v56, -|v42|
	v_exp_f32_e64 v57, -|v43|
	v_max_f32_e32 v44, 0, v44
	v_add_f32_e32 v6, 1.0, v6
	v_add_f32_e32 v49, 1.0, v49
	v_add_f32_e32 v44, v44, v58
	v_log_f32_e32 v6, v6
	v_log_f32_e32 v49, v49
	v_cndmask_b32_e64 v50, 0, -v37, s[18:19]
	v_fma_f32 v37, v7, s68, -v37
	v_cndmask_b32_e64 v7, 0, -v44, s[34:35]
	v_fma_f32 v14, v14, s68, -v44
	v_cndmask_b32_e64 v44, 0, -v2, s[36:37]
	v_fma_f32 v15, v15, s68, -v2
	v_max_f32_e32 v2, 0, v4
	v_add_f32_e32 v4, 1.0, v9
	v_add_f32_e32 v54, 1.0, v54
	v_add_f32_e32 v55, 1.0, v55
	v_add_f32_e32 v56, 1.0, v56
	v_add_f32_e32 v57, 1.0, v57
	v_log_f32_e32 v4, v4
	v_log_f32_e32 v54, v54
	v_log_f32_e32 v55, v55
	v_log_f32_e32 v56, v56
	v_log_f32_e32 v57, v57
	v_max_f32_e32 v35, 0, v35
	v_add_f32_e32 v2, v2, v6
	v_add_f32_e32 v35, v35, v49
	v_cndmask_b32_e64 v45, 0, -v2, s[38:39]
	v_fma_f32 v16, v16, s68, -v2
	v_max_f32_e32 v2, 0, v8
	v_max_f32_e32 v40, 0, v40
	v_max_f32_e32 v41, 0, v41
	v_max_f32_e32 v42, 0, v42
	v_max_f32_e32 v43, 0, v43
	v_cndmask_b32_e64 v49, 0, -v35, s[14:15]
	v_add_f32_e32 v2, v2, v4
	v_add_f32_e32 v40, v40, v54
	v_add_f32_e32 v41, v41, v55
	v_add_f32_e32 v42, v42, v56
	v_add_f32_e32 v43, v43, v57
	v_cndmask_b32_e64 v56, 0, -v2, s[40:41]
	v_fma_f32 v17, v17, s68, -v2
	v_add_f32_e32 v2, v46, v47
	v_add_f32_e32 v4, v48, v49
	v_fma_f32 v35, v5, s68, -v35
	v_cndmask_b32_e64 v5, 0, -v40, s[24:25]
	v_cndmask_b32_e64 v53, 0, -v41, s[26:27]
	v_cndmask_b32_e64 v54, 0, -v42, s[28:29]
	v_cndmask_b32_e64 v55, 0, -v43, s[30:31]
	v_add_f32_e32 v2, v2, v4
	v_add_f32_e32 v3, v3, v50
	v_add_f32_e32 v4, v51, v52
	v_add_f32_e32 v4, v3, v4
	v_add_f32_e32 v3, v5, v53
	v_add_f32_e32 v5, v54, v55
	v_add_f32_e32 v6, v3, v5
	v_add_f32_e32 v3, v7, v44
	v_add_f32_e32 v5, v45, v56
	v_add_f32_e32 v7, v3, v5
	v_fma_f32 v42, v12, s68, -v42
	v_fma_f32 v43, v13, s68, -v43
	v_mov_b32_e32 v12, v6
	v_mov_b32_e32 v13, v7
	s_nop 0
	v_permlane32_swap_b32_e32 v6, v12
	v_permlane32_swap_b32_e32 v7, v13
	v_fma_f32 v40, v10, s68, -v40
	v_mov_b32_e32 v10, v4
	v_pk_add_f32 v[6:7], v[6:7], v[12:13]
	v_fma_f32 v41, v11, s68, -v41
	v_permlane32_swap_b32_e32 v4, v10
	v_mov_b32_e32 v5, v6
	v_mov_b32_e32 v11, v7
	v_mov_b32_e32 v8, v2
	v_pk_add_f32 v[4:5], v[4:5], v[10:11]
	s_nop 0
	v_permlane32_swap_b32_e32 v2, v8
	v_mov_b32_e32 v3, v4
	v_mov_b32_e32 v9, v5
	v_pk_add_f32 v[66:67], v[2:3], v[8:9]
	v_cndmask_b32_e64 v3, 0, v8, s[6:7]
	v_add_f32_e32 v2, 0, v67
	v_add_f32_e32 v2, v3, v2
	v_add_f32_e32 v3, v49, v2
	v_add_f32_e32 v2, v35, v2
	v_add_f32_e32 v2, v153, v2
	v_add_f32_e32 v4, v48, v3
	v_exp_f32_e32 v8, v2
	v_add_f32_e32 v2, v34, v3
	v_add_f32_e32 v6, v47, v4
	v_add_f32_e32 v2, v152, v2
	v_exp_f32_e32 v3, v2
	v_add_f32_e32 v2, v33, v4
	v_add_f32_e32 v4, v32, v6
	v_add_f32_e32 v5, 0, v5
	v_cndmask_b32_e64 v6, 0, v10, s[6:7]
	v_add_f32_e32 v5, v6, v5
	v_add_f32_e32 v6, v52, v5
	v_add_f32_e32 v9, v51, v6
	v_add_f32_e32 v5, v39, v5
	v_add_f32_e32 v6, v38, v6
	v_add_f32_e32 v13, 0, v13
	v_add_f32_e32 v5, v157, v5
	v_add_f32_e32 v6, v156, v6
	v_add_f32_e32 v7, 0, v7
	v_cndmask_b32_e64 v11, 0, v12, s[6:7]
	v_cndmask_b32_e64 v13, 0, v13, s[6:7]
	v_exp_f32_e32 v5, v5
	v_exp_f32_e32 v6, v6
	v_add_f32_e32 v7, v11, v7
	v_add_f32_e32 v33, v56, v13
	v_add_f32_e32 v11, v55, v7
	v_add_f32_e32 v34, v45, v33
	v_add_f32_e32 v12, v54, v11
	v_add_f32_e32 v35, v44, v34
	v_add_f32_e32 v10, v50, v9
	v_add_f32_e32 v32, v53, v12
	v_add_f32_e32 v15, v15, v34
	v_add_f32_e32 v14, v14, v35
	v_add_f32_e32 v9, v37, v9
	v_add_f32_e32 v10, v36, v10
	v_add_f32_e32 v7, v43, v7
	v_add_f32_e32 v11, v42, v11
	v_add_f32_e32 v12, v41, v12
	v_add_f32_e32 v32, v40, v32
	v_add_f32_e32 v13, v17, v13
	v_add_f32_e32 v16, v16, v33
	v_add_f32_e32 v15, v163, v15
	v_cvt_pk_bf16_f32 v5, v6, v5
	v_add_f32_e32 v6, v162, v14
	v_add_f32_e32 v2, v151, v2
	v_add_f32_e32 v4, v150, v4
	v_add_f32_e32 v9, v155, v9
	v_add_f32_e32 v10, v154, v10
	v_add_f32_e32 v7, v161, v7
	v_add_f32_e32 v11, v160, v11
	v_add_f32_e32 v12, v159, v12
	v_add_f32_e32 v32, v158, v32
	v_add_f32_e32 v13, v165, v13
	v_add_f32_e32 v16, v164, v16
	v_exp_f32_e32 v15, v15
	v_exp_f32_e32 v6, v6
	v_exp_f32_e32 v2, v2
	v_exp_f32_e32 v4, v4
	v_exp_f32_e32 v9, v9
	v_exp_f32_e32 v10, v10
	v_exp_f32_e32 v7, v7
	v_exp_f32_e32 v11, v11
	v_exp_f32_e32 v12, v12
	v_exp_f32_e32 v32, v32
	v_exp_f32_e32 v13, v13
	v_cvt_pk_bf16_f32 v3, v3, v8
	v_exp_f32_e32 v8, v16
	v_add_co_u32_e32 v14, vcc, s49, v30
	v_cvt_pk_bf16_f32 v70, v6, v15
	s_nop 0
	v_addc_co_u32_e32 v15, vcc, 0, v31, vcc
	v_cvt_pk_bf16_f32 v2, v4, v2
	v_cvt_pk_bf16_f32 v4, v10, v9
	v_cvt_pk_bf16_f32 v68, v32, v12
	v_cvt_pk_bf16_f32 v69, v11, v7
	v_cvt_pk_bf16_f32 v71, v8, v13
	s_waitcnt vmcnt(7)
	v_mfma_f32_32x32x16_bf16 v[50:65], v[26:29], v[2:5], 0
	v_add_f32_e32 v67, v66, v67
	v_cmp_gt_f32_e32 vcc, s69, v67
	s_cmp_eq_u64 vcc, exec
	s_cselect_b64 s[64:65], -1, 0
	s_cmpk_gt_i32 s42, 0xfe
	s_cselect_b64 s[72:73], -1, 0
	s_waitcnt vmcnt(5)
	v_mfma_f32_32x32x16_bf16 v[34:49], v[18:21], v[2:5], 0
	s_or_b64 s[64:65], s[72:73], s[64:65]
	s_and_b64 vcc, exec, s[64:65]
	v_mfma_f32_32x32x16_bf16 v[50:65], v[22:25], v[68:71], v[50:65]
	s_waitcnt vmcnt(4)
	v_mfma_f32_32x32x16_bf16 v[34:49], v[244:247], v[68:71], v[34:49]
	s_waitcnt vmcnt(3)
	v_mfma_f32_32x32x16_bf16 v[18:33], v[248:251], v[2:5], 0
	s_waitcnt vmcnt(1)
	v_mfma_f32_32x32x16_bf16 v[18:33], v[236:239], v[68:71], v[18:33]
	s_waitcnt vmcnt(0)
	v_mfma_f32_32x32x16_bf16 v[2:17], v[240:243], v[2:5], 0
	v_mfma_f32_32x32x16_bf16 v[2:17], v[232:235], v[68:71], v[2:17]
	s_cbranch_vccnz .LBB0_1655
	v_sub_u32_e64 v66, s43, 1 clamp
	s_sub_i32 s63, 0xfe, s42
	v_add_f32_e32 v147, 0, v67
	s_add_i32 s64, s42, 0xffffff02
